# speedup vs baseline: 1.0066x; 1.0037x over previous
_Z9qsim_mainPKDF16_PK15HIP_vector_typeIfLj2EEPf:
	s_cmpk_gt_i32 s2, 0x3ff
	s_cbranch_scc1 .LBB1_11
	s_load_dwordx4 s[8:11], s[0:1], 0x0
	s_load_dwordx2 s[4:5], s[0:1], 0x10
	s_mul_i32 s1, s2, 56
	s_mul_hi_i32 s0, s2, 56
	v_mbcnt_lo_u32_b32 v2, -1, 0
	s_waitcnt lgkmcnt(0)
	s_add_u32 s6, s8, 0x20000
	s_addc_u32 s7, s9, 0
	s_add_u32 s20, s8, 0x80000
	s_addc_u32 s21, s9, 0
	s_add_u32 s12, s8, 0x38000
	s_addc_u32 s13, s9, 0
	s_add_i32 s22, s2, 0xfffffe00
	s_add_u32 s14, s4, s1
	s_addc_u32 s15, s5, s0
	s_mul_hi_i32 s0, s2, 0xa00
	s_mulk_i32 s2, 0xa00
	v_mbcnt_hi_u32_b32 v161, -1, v2
	s_add_u32 s10, s10, s2
	v_and_b32_e32 v2, 64, v161
	s_addc_u32 s11, s11, s0
	v_mov_b32_e32 v155, 0
	s_movk_i32 s23, 0x1000
	s_mov_b64 s[16:17], 0x28000
	v_mov_b32_e32 v1, 0x10000
	s_movk_i32 s24, 0x100
	v_mov_b32_e32 v158, 0x60
	v_mov_b32_e32 v159, 0x280
	v_mov_b32_e32 v160, 0x1280
	s_mov_b64 s[18:19], 0x40000
	s_mov_b32 s25, 0x40000
	v_xor_b32_e32 v162, 32, v161
	v_add_u32_e32 v163, 64, v2
	v_xor_b32_e32 v164, 16, v161
	v_mov_b32_e32 v165, 0x10a00
	v_mov_b32_e32 v156, v0
	v_and_b32_e32 v167, 63, v0
	v_ashrrev_i32_e32 v157, 31, v156
	v_lshlrev_b32_e32 v169, 3, v167
	v_lshl_add_u64 v[6:7], v[156:157], 3, s[10:11]
	global_load_dwordx2 v[4:5], v[6:7], off
	global_load_dwordx2 v[2:3], v169, s[10:11] offset:2048
	v_lshlrev_b32_e32 v8, 4, v167
	v_add_u32_e32 v9, 0x1000, v8
	global_load_dwordx4 v[222:225], v8, s[6:7]
	global_load_dwordx4 v[226:229], v8, s[6:7] offset:1024
	global_load_dwordx4 v[230:233], v8, s[6:7] offset:2048
	global_load_dwordx4 v[234:237], v8, s[6:7] offset:3072
	global_load_dwordx4 v[238:241], v9, s[6:7]
	global_load_dwordx4 v[242:245], v9, s[6:7] offset:1024
	global_load_dwordx4 v[246:249], v9, s[6:7] offset:2048
	global_load_dwordx4 v[250:253], v9, s[6:7] offset:3072
	s_nop 0
	s_nop 0
	s_branch .LBB1_3

.LBB1_3:
	v_mov_b32_e32 v156, v0
	s_nop 0
	v_ashrrev_i32_e32 v157, 31, v156
	v_and_b32_e32 v167, 63, v156
	v_lshl_add_u64 v[6:7], v[156:157], 3, s[10:11]
	v_lshlrev_b32_e32 v169, 3, v167
	v_readfirstlane_b32 s4, v156
	s_ashr_i32 s27, s4, 7
	s_lshl_b32 s0, s27, 1
	s_ashr_i32 s1, s0, 31
	s_lshl_b64 s[2:3], s[0:1], 13
	s_add_u32 s2, s8, s2
	s_addc_u32 s3, s9, s3
	s_add_u32 s28, s2, 0x18000
	s_addc_u32 s29, s3, 0
	v_lshlrev_b32_e32 v154, 4, v167
	v_lshl_add_u64 v[6:7], s[28:29], 0, v[154:155]
	v_or_b32_e32 v8, 0x800, v169
	v_add_co_u32_e32 v6, vcc, s23, v6
	v_lshlrev_b32_e32 v168, 1, v8
	s_nop 0
	v_addc_co_u32_e32 v7, vcc, 0, v7, vcc
	global_load_dwordx4 v[150:153], v154, s[28:29]
	global_load_dwordx4 v[146:149], v154, s[28:29] offset:1024
	global_load_dwordx4 v[142:145], v154, s[28:29] offset:2048
	global_load_dwordx4 v[138:141], v154, s[28:29] offset:3072
	global_load_dwordx4 v[126:129], v[6:7], off offset:1024
	global_load_dwordx4 v[122:125], v[6:7], off offset:2048
	global_load_dwordx4 v[134:137], v168, s[28:29]
	global_load_dwordx4 v[130:133], v[6:7], off offset:3072
	v_lshl_add_u64 v[6:7], s[2:3], 0, v[154:155]
	v_lshl_add_u64 v[8:9], v[6:7], 0, s[16:17]
	v_add_co_u32_e32 v6, vcc, 0x28000, v6
	s_nop 1
	v_addc_co_u32_e32 v7, vcc, 0, v7, vcc
	global_load_dwordx4 v[86:89], v[6:7], off
	global_load_dwordx4 v[82:85], v[8:9], off offset:1024
	v_lshl_add_u32 v166, v156, 2, v165
	s_cmp_lt_i32 s22, 0
	s_cbranch_scc0 .Lskip_stage0
	v_lshl_add_u32 v6, v156, 3, v1
	v_cmp_gt_i32_e32 vcc, 64, v156
	s_waitcnt vmcnt(19)
	ds_write_b64 v6, v[4:5]
	s_and_saveexec_b64 s[2:3], vcc
	s_cbranch_execz .LBB1_7
	s_waitcnt vmcnt(18)
	ds_write_b64 v6, v[2:3] offset:2048
.LBB1_7:
	s_or_b64 exec, exec, s[2:3]
	s_waitcnt vmcnt(18) lgkmcnt(0)
	s_barrier
